# retention past-state loop: the second half-iteration waited for the loads it had just issued (compiler merged the waitcnt of the load/no-load paths); counts relaxed to 7/6/4 with a drained stub on the
# speedup vs baseline: 1.0056x; 1.0056x over previous
; #define ATT_LOAD(T, jt) do { const int s0_ = (jt) * 64; const bf16* kr_ = kbase + (size_t)s0_ * 1024; T.ka = *(const u32x4*)kr_; T.kb = *(const u32x4*)(kr_ + 64); \
;         T.va = *(const u32x4*)(vbase + s0_); T.vb = *(const u32x4*)(vbase + s0_ + 8); } while (0)
; #define P1_STORE(T, buf, jt) do { const float dec_ = __builtin_amdgcn_exp2f((float)(t0 - (jt) * 64 - kkey) * lg2); const u32x4 ka_ = scale8(T.ka, dec_), kb_ = scale8(T.kb, dec_); ATT_STORE(T, buf, ka_, kb_); } while (0)
; template <int BR>
; DI void unit(LAS unsigned char* lds, const bf16* __restrict__ Q, const bf16* __restrict__ Kx, const bf16* __restrict__ VT, const bf16* __restrict__ RG, const bf16* __restrict__ RG1, bf16* __restrict__ O, int b, int h, int qb) {
;     ...
;         const int np = 4 * qb;
;         ATT_LOAD(ta, 0); ATT_LOAD(tb, 1);
;         for (int jt = 0; jt < np; jt += 2) {
;             P1_STORE(ta, 0, jt);
;             __syncthreads();
;             if (jt + 2 < np) ATT_LOAD(ta, jt + 2);
;             P1_COMPUTE(0);
;             P1_STORE(tb, 1, jt + 1);
;             __syncthreads();
;             if (jt + 3 < np) ATT_LOAD(tb, jt + 3);
;             P1_COMPUTE(1);
;         }
.LBB0_403:
	v_add_u32_e32 v128, 0x8800, v91
	v_add_u32_e32 v136, 0x9900, v91
	ds_read_b64_tr_b16 v[92:93], v90
	ds_read_b64_tr_b16 v[94:95], v90 offset:1088
	ds_read2_b64 v[128:131], v128 offset1:1
	ds_read_b64_tr_b16 v[132:133], v90 offset:4352
	ds_read_b64_tr_b16 v[134:135], v90 offset:5440
	ds_read2_b64 v[136:139], v136 offset1:1
	v_add_u32_e32 v140, 0x9940, v91
	s_waitcnt lgkmcnt(3)
	v_mfma_f32_32x32x16_bf16 v[16:31], v[92:95], v[128:131], v[16:31]
	v_add_u32_e32 v128, 0x8820, v91
	v_add_u32_e32 v129, 0x9920, v91
	v_subrev_u32_e32 v146, 64, v71
	v_cvt_f32_i32_e32 v146, v146
	v_add_u32_e32 v151, 0x8860, v91
	v_add_u32_e32 v153, 0x9960, v91
	s_waitcnt vmcnt(7)
	v_lshlrev_b32_e32 v160, 16, v48
	s_waitcnt lgkmcnt(0)
	v_mfma_f32_32x32x16_bf16 v[0:15], v[92:95], v[136:139], v[0:15]
	ds_read2_b64 v[92:95], v128 offset1:1
	ds_read2_b64 v[128:131], v129 offset1:1
	v_add_u32_e32 v136, 0x8840, v91
	ds_read2_b64 v[136:139], v136 offset1:1
	ds_read2_b64 v[140:143], v140 offset1:1
	v_mul_f32_e32 v146, v150, v146
	v_exp_f32_e32 v146, v146
	v_and_b32_e32 v161, 0xffff0000, v48
	v_lshlrev_b32_e32 v162, 16, v49
	s_waitcnt lgkmcnt(3)
	v_mfma_f32_32x32x16_bf16 v[16:31], v[132:135], v[92:95], v[16:31]
	ds_read_b64_tr_b16 v[92:93], v90 offset:8704
	ds_read_b64_tr_b16 v[94:95], v90 offset:9792
	ds_read_b64_tr_b16 v[156:157], v90 offset:13056
	ds_read_b64_tr_b16 v[158:159], v90 offset:14144
	v_and_b32_e32 v163, 0xffff0000, v49
	v_pk_mul_f32 v[160:161], v[146:147], v[160:161] op_sel_hi:[0,1]
	v_pk_mul_f32 v[162:163], v[146:147], v[162:163] op_sel_hi:[0,1]
	s_add_i32 s11, s11, 3
	s_cmp_ge_u32 s11, s10
	s_waitcnt lgkmcnt(6)
	v_mfma_f32_32x32x16_bf16 v[0:15], v[132:135], v[128:131], v[0:15]
	ds_read2_b64 v[128:131], v151 offset1:1
	ds_read2_b64 v[132:135], v153 offset1:1
	s_waitcnt lgkmcnt(4)
	v_mfma_f32_32x32x16_bf16 v[16:31], v[92:95], v[136:139], v[16:31]
	v_lshlrev_b32_e32 v136, 16, v50
	v_and_b32_e32 v137, 0xffff0000, v50
	v_mul_f32_e64 v138, v146, v136
	v_mul_f32_e64 v139, v146, v137
	v_lshlrev_b32_e32 v136, 16, v51
	v_and_b32_e32 v137, 0xffff0000, v51
	v_pk_mul_f32 v[164:165], v[146:147], v[136:137] op_sel_hi:[0,1]
	v_cvt_pk_bf16_f32 v136, v160, v161
	v_mfma_f32_32x32x16_bf16 v[0:15], v[92:95], v[140:143], v[0:15]
	s_waitcnt vmcnt(6)
	v_lshlrev_b32_e32 v92, 16, v52
	v_and_b32_e32 v93, 0xffff0000, v52
	v_mul_f32_e64 v92, v146, v92
	v_mul_f32_e64 v93, v146, v93
	v_lshlrev_b32_e32 v94, 16, v53
	v_and_b32_e32 v95, 0xffff0000, v53
	v_cvt_pk_bf16_f32 v137, v162, v163
	v_cvt_pk_bf16_f32 v138, v138, v139
	s_waitcnt lgkmcnt(1)
	v_mfma_f32_32x32x16_bf16 v[16:31], v[156:159], v[128:131], v[16:31]
	v_lshlrev_b32_e32 v128, 16, v54
	v_and_b32_e32 v129, 0xffff0000, v54
	v_lshlrev_b32_e32 v130, 16, v55
	v_and_b32_e32 v131, 0xffff0000, v55
	v_cvt_pk_bf16_f32 v139, v164, v165
	v_pk_mul_f32 v[94:95], v[146:147], v[94:95] op_sel_hi:[0,1]
	v_pk_mul_f32 v[128:129], v[146:147], v[128:129] op_sel_hi:[0,1]
	s_waitcnt lgkmcnt(0)
	v_mfma_f32_32x32x16_bf16 v[0:15], v[156:159], v[132:135], v[0:15]
	v_mul_f32_e64 v130, v146, v130
	v_mul_f32_e64 v131, v146, v131
	v_cvt_pk_bf16_f32 v92, v92, v93
	v_cvt_pk_bf16_f32 v93, v94, v95
	v_cvt_pk_bf16_f32 v94, v128, v129
	v_cvt_pk_bf16_f32 v95, v130, v131
	ds_write_b128 v88, v[136:139] offset:17408
	ds_write_b128 v88, v[92:95] offset:17536
	v_add_u32_e32 v92, 0xcc00, v89
	s_waitcnt vmcnt(4)
	ds_write2_b64 v92, v[60:61], v[62:63] offset1:1
	v_add_u32_e32 v92, 0xcc10, v89
	ds_write2_b64 v92, v[56:57], v[58:59] offset1:1
	s_waitcnt lgkmcnt(0)
	s_barrier
	s_cbranch_scc1 .LBB0_400
	v_add_co_u32_e32 v52, vcc, 0x19b60000, v78
	s_nop 1
	v_addc_co_u32_e32 v53, vcc, 0, v79, vcc
	global_load_dwordx4 v[48:51], v[52:53], off
	s_nop 0
	global_load_dwordx4 v[52:55], v[52:53], off offset:128
	s_nop 0
	global_load_dwordx4 v[56:59], v[76:77], off offset:16
	global_load_dwordx4 v[60:63], v[76:77], off
	s_branch .LBB0_400
.Lmy_p1skip_0:
	s_waitcnt vmcnt(0)
	s_branch .LBB0_403
